# speedup vs baseline: 1.0032x; 1.0032x over previous
_Z8knn_gemmPKcS0_Pi:
	s_ashr_i32 s3, s2, 31
	s_lshr_b32 s3, s3, 29
	s_add_i32 s3, s2, s3
	s_ashr_i32 s4, s3, 3
	s_and_b32 s3, s3, -8
	s_sub_i32 s3, s2, s3
	s_cmp_lt_i32 s3, 0
	s_movk_i32 s12, 0x188
	s_cselect_b32 s5, s12, 0x187
	s_mul_i32 s3, s5, s3
	s_add_i32 s3, s3, s4
	s_ashr_i32 s4, s3, 31
	s_lshr_b32 s4, s4, 27
	s_add_i32 s10, s3, s4
	s_ashr_i32 s4, s10, 5
	s_lshl_b32 s11, s4, 2
	s_sub_i32 s4, 0x187, s11
	s_min_i32 s13, s4, 4
	s_abs_i32 s14, s13
	v_cvt_f32_u32_e32 v1, s14
	s_andn2_b32 s10, s10, 31
	s_load_dwordx4 s[4:7], s[0:1], 0x0
	s_load_dwordx2 s[8:9], s[0:1], 0x10
	s_sub_i32 s0, s3, s10
	v_rcp_iflag_f32_e32 v1, v1
	s_sub_i32 s10, 0, s14
	s_abs_i32 s3, s0
	s_xor_b32 s1, s0, s13
	v_mul_f32_e32 v1, 0x4f7ffffe, v1
	v_cvt_u32_f32_e32 v1, v1
	s_ashr_i32 s1, s1, 31
	v_lshrrev_b32_e32 v2, 8, v0
	v_lshlrev_b32_e32 v168, 4, v0
	v_readfirstlane_b32 s15, v1
	s_mul_i32 s10, s10, s15
	s_mul_hi_u32 s10, s15, s10
	s_add_i32 s15, s15, s10
	s_mul_hi_u32 s10, s3, s15
	s_mul_i32 s15, s10, s14
	s_sub_i32 s3, s3, s15
	s_add_i32 s15, s10, 1
	s_sub_i32 s16, s3, s14
	s_cmp_ge_u32 s3, s14
	s_cselect_b32 s10, s15, s10
	s_cselect_b32 s3, s16, s3
	s_add_i32 s15, s10, 1
	s_cmp_ge_u32 s3, s14
	s_cselect_b32 s3, s15, s10
	s_xor_b32 s3, s3, s1
	s_sub_i32 s34, s3, s1
	s_mul_i32 s1, s34, s13
	s_sub_i32 s0, s0, s1
	s_add_i32 s11, s11, s0
	v_readfirstlane_b32 s1, v0
	s_sub_i32 s13, 0x186, s11
	s_lshl_b32 s3, s1, 4
	s_mul_i32 s10, s34, 0x30000
	s_mul_hi_i32 s1, s34, 0x30000
	s_waitcnt lgkmcnt(0)
	s_add_u32 s10, s6, s10
	s_addc_u32 s11, s7, s1
	s_mul_i32 s14, s13, 0x30000
	s_mul_hi_i32 s1, s13, 0x30000
	s_add_u32 s22, s4, s14
	v_readfirstlane_b32 s0, v2
	s_addc_u32 s23, s5, s1
	s_cmp_eq_u32 s0, 0
	s_cselect_b64 s[0:1], -1, 0
	s_add_u32 s16, s10, 0x2000
	s_addc_u32 s17, s11, 0
	s_add_u32 s18, s22, 0xfffff000
	s_addc_u32 s19, s23, -1
	s_and_b64 s[14:15], s[0:1], exec
	s_cselect_b32 s17, s17, s19
	s_cselect_b32 s16, s16, s18
	s_add_u32 s18, s22, 0x1000
	s_addc_u32 s19, s23, 0
	s_add_i32 s14, s3, 0
	s_mov_b64 s[20:21], s[10:11]
	s_add_i32 s15, s14, 0x2000
	v_lshrrev_b32_e32 v5, 2, v0
	v_lshrrev_b32_e32 v1, 4, v0
	s_add_i32 s16, s14, 0x4000
	v_and_b32_e32 v5, 2, v5
	s_add_u32 s18, s10, 0x3000
	s_addc_u32 s19, s11, 0
	s_add_u32 s3, s10, 0x5000
	s_addc_u32 s17, s11, 0
	s_add_u32 s20, s22, 0x2000
	s_addc_u32 s21, s23, 0
	s_and_b64 s[10:11], s[0:1], exec
	s_cselect_b32 s11, s17, s21
	s_cselect_b32 s10, s3, s20
	s_add_u32 s20, s22, 0x4000
	s_addc_u32 s21, s23, 0
	s_add_i32 s17, s14, 0x6000
	v_add_lshl_u32 v1, v5, v1, 3
	s_add_i32 s18, s14, 0x8000
	s_add_i32 s19, s14, 0xa000
	v_and_b32_e32 v3, 15, v0
	v_and_b32_e32 v5, 24, v1
	v_lshrrev_b32_e32 v1, 1, v0
	s_movk_i32 s3, 0x60
	s_add_i32 s20, s14, 0xc000
	v_and_or_b32 v1, v1, s3, v3
	v_lshl_or_b32 v2, v2, 6, v3
	s_add_u32 s21, s4, 0x12000
	v_and_b32_e32 v4, 48, v0
	v_mad_u32_u24 v6, v1, s3, 0
	v_mad_u32_u24 v2, v2, s3, 0
	s_addc_u32 s22, s5, 0
	v_add_u32_e32 v1, v6, v4
	v_add_u32_e32 v170, v2, v4
	v_add_u32_e32 v172, v6, v5
	v_add_u32_e32 v173, v2, v5
	v_mov_b32_e32 v39, 0
	s_add_u32 s23, s6, 0x12000
	v_add_u32_e32 v171, 0x3000, v170
	v_add_u32_e32 v174, 0x3040, v173
	v_mov_b32_e32 v169, v39
	v_add_u32_e32 v175, 0x12000, v1
	v_add_u32_e32 v176, 0x12040, v172
	v_add_u32_e32 v177, 0x15000, v170
	v_add_u32_e32 v178, 0x15040, v173
	v_add_u32_e32 v179, 0x12600, v1
	v_add_u32_e32 v180, 0x12640, v172
	v_add_u32_e32 v181, 0x15600, v170
	v_add_u32_e32 v182, 0x15640, v173
	v_add_u32_e32 v183, 0x15c00, v170
	v_add_u32_e32 v184, 0x15c40, v173
	v_add_u32_e32 v185, 0x16200, v170
	v_add_u32_e32 v186, 0x16240, v173
	s_addc_u32 s24, s7, 0
	v_mov_b32_e32 v187, 0x7f7f7f7f
	s_add_i32 s25, 0, 0x18000
	s_movk_i32 s26, 0xff80
	s_movk_i32 s27, 0x30e
	s_add_i32 s28, s14, 0xe000
	s_add_i32 s29, s20, 0x4000
	s_add_i32 s30, s14, 0x12000
	s_add_i32 s31, s14, 0x14000
	s_add_i32 s33, s14, 0x16000
	s_lshr_b32 s66, s14, 12
	s_and_b32 s54, s14, 0xfff
	s_mul_i32 s67, s66, 0x6000
	s_add_i32 s54, s54, s67
	s_add_i32 s55, s54, 0x1000
	s_add_i32 s56, s54, 0x2000
	s_add_i32 s57, s54, 0x3000
	s_add_i32 s58, s54, 0x4000
	s_add_i32 s59, s54, 0x5000
	s_add_i32 s60, s54, 0xc000
	s_add_i32 s61, s54, 0xd000
	s_add_i32 s62, s54, 0xe000
	s_add_i32 s63, s54, 0xf000
	s_add_i32 s64, s54, 0x10000
	s_add_i32 s65, s54, 0x11000
	v_and_b32_e32 v228, 0xfff, v168
	v_add_u32_e32 v229, 0x1000, v228
	v_add_u32_e32 v230, 0x2000, v228
	s_mul_i32 s68, s34, 0x30000
	s_mul_hi_i32 s69, s34, 0x30000
	s_add_u32 s68, s6, s68
	s_addc_u32 s69, s7, s69
	s_mul_i32 s70, s13, 0x30000
	s_mul_hi_i32 s71, s13, 0x30000
	s_add_u32 s70, s4, s70
	s_addc_u32 s71, s5, s71
	s_mul_i32 s67, s66, 0x3000
	s_add_u32 s68, s68, s67
	s_addc_u32 s69, s69, 0
	s_add_u32 s70, s70, s67
	s_addc_u32 s71, s71, 0
	s_mov_b32 m0, s54
	s_nop 0
	global_load_lds_dwordx4 v228, s[68:69]
	s_mov_b32 m0, s55
	s_nop 0
	global_load_lds_dwordx4 v229, s[68:69]
	s_mov_b32 m0, s56
	s_nop 0
	global_load_lds_dwordx4 v230, s[68:69]
	s_mov_b32 m0, s57
	s_nop 0
	global_load_lds_dwordx4 v228, s[70:71]
	s_mov_b32 m0, s58
	s_nop 0
	global_load_lds_dwordx4 v229, s[70:71]
	s_mov_b32 m0, s59
	s_nop 0
	global_load_lds_dwordx4 v230, s[70:71]
	s_branch .LBB1_2

.LBB1_2:
	s_mul_i32 s41, s34, 0x30000
	s_mul_hi_i32 s40, s34, 0x30000
	s_add_u32 s11, s6, s41
	s_addc_u32 s35, s7, s40
	s_mov_b32 s10, s2
	s_add_u32 s2, s11, 0x6000
	s_addc_u32 s3, s35, 0
	s_mul_i32 s43, s13, 0x30000
	s_mul_hi_i32 s42, s13, 0x30000
	s_add_u32 s44, s4, s43
	s_addc_u32 s45, s5, s42
	s_add_u32 s38, s11, 0x8000
	s_addc_u32 s39, s35, 0
	s_add_u32 s46, s44, 0x5000
	s_addc_u32 s47, s45, 0
	s_and_b64 s[36:37], s[0:1], exec
	s_cselect_b32 s37, s39, s47
	s_cselect_b32 s36, s38, s46
	s_add_u32 s38, s44, 0x7000
	s_addc_u32 s39, s45, 0
	s_waitcnt vmcnt(0)
	s_barrier
	s_add_u32 s2, s11, 0x9000
	s_addc_u32 s3, s35, 0
	s_add_u32 s11, s11, 0xb000
	s_addc_u32 s35, s35, 0
	s_add_u32 s38, s44, 0x8000
	s_addc_u32 s39, s45, 0
	s_and_b64 s[36:37], s[0:1], exec
	s_cselect_b32 s37, s35, s39
	s_cselect_b32 s36, s11, s38
	s_add_u32 s38, s44, 0xa000
	s_addc_u32 s39, s45, 0
	s_add_u32 s11, s21, s43
	s_addc_u32 s35, s22, s42
	ds_read_b128 v[2:5], v170 offset:12288
	ds_read_b64 v[6:7], v173 offset:12352
	ds_read_b128 v[8:11], v170 offset:13824
	ds_read_b64 v[12:13], v173 offset:13888
	ds_read_b128 v[14:17], v170 offset:15360
	ds_read_b64 v[18:19], v173 offset:15424
	ds_read_b128 v[26:29], v170 offset:16896
	ds_read_b64 v[30:31], v173 offset:16960
	ds_read_b128 v[20:23], v1
	ds_read_b64 v[24:25], v172 offset:64
	ds_read_b128 v[32:35], v1 offset:1536
	ds_read_b64 v[36:37], v172 offset:1600
	s_add_u32 s68, s6, s41
	s_addc_u32 s69, s7, s40
	s_add_u32 s70, s4, s43
	s_addc_u32 s71, s5, s42
	s_mul_i32 s67, s66, 0x3000
	s_add_i32 s67, s67, 0x6000
	s_add_u32 s68, s68, s67
	s_addc_u32 s69, s69, 0
	s_add_u32 s70, s70, s67
	s_addc_u32 s71, s71, 0
	s_mov_b32 m0, s60
	s_nop 0
	global_load_lds_dwordx4 v228, s[68:69]
	s_mov_b32 m0, s61
	s_nop 0
	global_load_lds_dwordx4 v229, s[68:69]
	s_mov_b32 m0, s62
	s_nop 0
	global_load_lds_dwordx4 v230, s[68:69]
	s_mov_b32 m0, s63
	s_nop 0
	global_load_lds_dwordx4 v228, s[70:71]
	s_mov_b32 m0, s64
	s_nop 0
	global_load_lds_dwordx4 v229, s[70:71]
	s_mov_b32 m0, s65
	s_nop 0
	global_load_lds_dwordx4 v230, s[70:71]
	s_add_u32 s2, s23, s41
	s_addc_u32 s3, s24, s40
	s_mov_b32 s36, -2
	s_waitcnt lgkmcnt(0)
.Lgemm_peel:
	ds_read_b128 v[188:191], v1 offset:24576
	ds_read_b64 v[192:193], v172 offset:24640
	ds_read_b128 v[194:197], v1 offset:26112
	ds_read_b64 v[198:199], v172 offset:26176
	ds_read_b128 v[200:203], v170 offset:36864
	ds_read_b64 v[204:205], v173 offset:36928
	ds_read_b128 v[206:209], v170 offset:38400
	ds_read_b64 v[210:211], v173 offset:38464
	ds_read_b128 v[212:215], v170 offset:39936
	ds_read_b64 v[216:217], v173 offset:40000
	ds_read_b128 v[218:221], v170 offset:41472
	ds_read_b64 v[222:223], v173 offset:41536
	s_setprio 1
	v_mfma_scale_f32_16x16x128_f8f6f4 v[164:167], v[2:7], v[20:25], 0, v187, v187 op_sel_hi:[0,0,0] cbsz:2 blgp:2
	v_mfma_scale_f32_16x16x128_f8f6f4 v[160:163], v[8:13], v[20:25], 0, v187, v187 op_sel_hi:[0,0,0] cbsz:2 blgp:2
	v_mfma_scale_f32_16x16x128_f8f6f4 v[156:159], v[14:19], v[20:25], 0, v187, v187 op_sel_hi:[0,0,0] cbsz:2 blgp:2
	v_mfma_scale_f32_16x16x128_f8f6f4 v[152:155], v[26:31], v[20:25], 0, v187, v187 op_sel_hi:[0,0,0] cbsz:2 blgp:2
	v_mfma_scale_f32_16x16x128_f8f6f4 v[148:151], v[2:7], v[32:37], 0, v187, v187 op_sel_hi:[0,0,0] cbsz:2 blgp:2
	v_mfma_scale_f32_16x16x128_f8f6f4 v[140:143], v[8:13], v[32:37], 0, v187, v187 op_sel_hi:[0,0,0] cbsz:2 blgp:2
	v_mfma_scale_f32_16x16x128_f8f6f4 v[132:135], v[14:19], v[32:37], 0, v187, v187 op_sel_hi:[0,0,0] cbsz:2 blgp:2
	v_mfma_scale_f32_16x16x128_f8f6f4 v[124:127], v[26:31], v[32:37], 0, v187, v187 op_sel_hi:[0,0,0] cbsz:2 blgp:2
	s_setprio 0
	s_cmp_eq_u32 s66, 0
	s_cbranch_scc0 .Lpst0_other
	s_add_u32 s38, s2, 0xffffa000
	s_addc_u32 s39, s3, -1
	s_add_u32 s40, s11, 0xffffa000
	s_addc_u32 s41, s35, -1
	s_waitcnt vmcnt(0)
	s_barrier
	s_mov_b32 m0, s54
	s_nop 0
	global_load_lds_dwordx4 v228, s[38:39]
	s_mov_b32 m0, s55
	s_nop 0
	global_load_lds_dwordx4 v229, s[38:39]
	s_mov_b32 m0, s56
	s_nop 0
	global_load_lds_dwordx4 v230, s[38:39]
	s_mov_b32 m0, s57
	s_nop 0
	global_load_lds_dwordx4 v228, s[40:41]
	s_mov_b32 m0, s58
	s_nop 0
	global_load_lds_dwordx4 v229, s[40:41]
	s_mov_b32 m0, s59
	s_nop 0
	global_load_lds_dwordx4 v230, s[40:41]
	s_branch .Lpst0_join
.Lpst0_other:
	s_barrier
.Lpst0_join:
	s_setprio 1
	s_waitcnt lgkmcnt(0)
	v_mfma_scale_f32_16x16x128_f8f6f4 v[112:115], v[2:7], v[188:193], 0, v187, v187 op_sel_hi:[0,0,0] cbsz:2 blgp:2
	v_mfma_scale_f32_16x16x128_f8f6f4 v[100:103], v[8:13], v[188:193], 0, v187, v187 op_sel_hi:[0,0,0] cbsz:2 blgp:2
	v_mfma_scale_f32_16x16x128_f8f6f4 v[92:95], v[14:19], v[188:193], 0, v187, v187 op_sel_hi:[0,0,0] cbsz:2 blgp:2
	v_mfma_scale_f32_16x16x128_f8f6f4 v[88:91], v[26:31], v[188:193], 0, v187, v187 op_sel_hi:[0,0,0] cbsz:2 blgp:2
	v_mfma_scale_f32_16x16x128_f8f6f4 v[84:87], v[2:7], v[194:199], 0, v187, v187 op_sel_hi:[0,0,0] cbsz:2 blgp:2
	v_mfma_scale_f32_16x16x128_f8f6f4 v[76:79], v[8:13], v[194:199], 0, v187, v187 op_sel_hi:[0,0,0] cbsz:2 blgp:2
	v_mfma_scale_f32_16x16x128_f8f6f4 v[68:71], v[14:19], v[194:199], 0, v187, v187 op_sel_hi:[0,0,0] cbsz:2 blgp:2
	v_mfma_scale_f32_16x16x128_f8f6f4 v[60:63], v[26:31], v[194:199], 0, v187, v187 op_sel_hi:[0,0,0] cbsz:2 blgp:2
	s_setprio 0
	ds_read_b128 v[2:5], v170 offset:61440
	ds_read_b64 v[6:7], v173 offset:61504
	ds_read_b128 v[8:11], v170 offset:62976
	ds_read_b64 v[12:13], v173 offset:63040
	ds_read_b128 v[14:17], v170 offset:64512
	ds_read_b64 v[18:19], v173 offset:64576
	ds_read_b128 v[26:29], v171 offset:53760
	ds_read_b64 v[30:31], v174 offset:53760
	s_setprio 1
	v_mfma_scale_f32_16x16x128_f8f6f4 v[144:147], v[200:205], v[20:25], 0, v187, v187 op_sel_hi:[0,0,0] cbsz:2 blgp:2
	v_mfma_scale_f32_16x16x128_f8f6f4 v[136:139], v[206:211], v[20:25], 0, v187, v187 op_sel_hi:[0,0,0] cbsz:2 blgp:2
	v_mfma_scale_f32_16x16x128_f8f6f4 v[128:131], v[212:217], v[20:25], 0, v187, v187 op_sel_hi:[0,0,0] cbsz:2 blgp:2
	v_mfma_scale_f32_16x16x128_f8f6f4 v[120:123], v[218:223], v[20:25], 0, v187, v187 op_sel_hi:[0,0,0] cbsz:2 blgp:2
	v_mfma_scale_f32_16x16x128_f8f6f4 v[116:119], v[200:205], v[32:37], 0, v187, v187 op_sel_hi:[0,0,0] cbsz:2 blgp:2
	v_mfma_scale_f32_16x16x128_f8f6f4 v[108:111], v[206:211], v[32:37], 0, v187, v187 op_sel_hi:[0,0,0] cbsz:2 blgp:2
	v_mfma_scale_f32_16x16x128_f8f6f4 v[104:107], v[212:217], v[32:37], 0, v187, v187 op_sel_hi:[0,0,0] cbsz:2 blgp:2
	v_mfma_scale_f32_16x16x128_f8f6f4 v[96:99], v[218:223], v[32:37], 0, v187, v187 op_sel_hi:[0,0,0] cbsz:2 blgp:2
	s_setprio 0
	ds_read_b128 v[20:23], v1 offset:49152
	ds_read_b64 v[24:25], v172 offset:49216
	ds_read_b128 v[32:35], v1 offset:50688
	ds_read_b64 v[36:37], v172 offset:50752
	s_cmp_eq_u32 s66, 1
	s_cbranch_scc0 .Lpst1_other
	s_add_u32 s38, s2, 0xffffd000
	s_addc_u32 s39, s3, -1
	s_add_u32 s40, s11, 0xffffd000
	s_addc_u32 s41, s35, -1
	s_waitcnt vmcnt(0)
	s_barrier
	s_mov_b32 m0, s54
	s_nop 0
	global_load_lds_dwordx4 v228, s[38:39]
	s_mov_b32 m0, s55
	s_nop 0
	global_load_lds_dwordx4 v229, s[38:39]
	s_mov_b32 m0, s56
	s_nop 0
	global_load_lds_dwordx4 v230, s[38:39]
	s_mov_b32 m0, s57
	s_nop 0
	global_load_lds_dwordx4 v228, s[40:41]
	s_mov_b32 m0, s58
	s_nop 0
	global_load_lds_dwordx4 v229, s[40:41]
	s_mov_b32 m0, s59
	s_nop 0
	global_load_lds_dwordx4 v230, s[40:41]
	s_branch .Lpst1_join

.Lpst1_join:
	s_setprio 1
	v_mfma_scale_f32_16x16x128_f8f6f4 v[80:83], v[200:205], v[188:193], 0, v187, v187 op_sel_hi:[0,0,0] cbsz:2 blgp:2
	v_mfma_scale_f32_16x16x128_f8f6f4 v[72:75], v[206:211], v[188:193], 0, v187, v187 op_sel_hi:[0,0,0] cbsz:2 blgp:2
	v_mfma_scale_f32_16x16x128_f8f6f4 v[64:67], v[212:217], v[188:193], 0, v187, v187 op_sel_hi:[0,0,0] cbsz:2 blgp:2
	v_mfma_scale_f32_16x16x128_f8f6f4 v[56:59], v[218:223], v[188:193], 0, v187, v187 op_sel_hi:[0,0,0] cbsz:2 blgp:2
	v_mfma_scale_f32_16x16x128_f8f6f4 v[52:55], v[200:205], v[194:199], 0, v187, v187 op_sel_hi:[0,0,0] cbsz:2 blgp:2
	v_mfma_scale_f32_16x16x128_f8f6f4 v[224:227], v[206:211], v[194:199], 0, v187, v187 op_sel_hi:[0,0,0] cbsz:2 blgp:2
	v_mfma_scale_f32_16x16x128_f8f6f4 v[212:215], v[212:217], v[194:199], 0, v187, v187 op_sel_hi:[0,0,0] cbsz:2 blgp:2
	v_mfma_scale_f32_16x16x128_f8f6f4 v[216:219], v[218:223], v[194:199], 0, v187, v187 op_sel_hi:[0,0,0] cbsz:2 blgp:2
	s_setprio 0
	s_waitcnt lgkmcnt(0)
	s_nop 0
	ds_read_b128 v[40:43], v175
	ds_read_b64 v[44:45], v176
	ds_read_b128 v[188:191], v179
	ds_read_b64 v[192:193], v180
	ds_read_b128 v[46:49], v177
	ds_read_b64 v[50:51], v178
	ds_read_b128 v[194:197], v181
	ds_read_b64 v[198:199], v182
	ds_read_b128 v[200:203], v183
	ds_read_b64 v[204:205], v184
	ds_read_b128 v[206:209], v185
	ds_read_b64 v[210:211], v186
	s_setprio 1
	v_mfma_scale_f32_16x16x128_f8f6f4 v[164:167], v[2:7], v[20:25], v[164:167], v187, v187 op_sel_hi:[0,0,0] cbsz:2 blgp:2
	v_mfma_scale_f32_16x16x128_f8f6f4 v[160:163], v[8:13], v[20:25], v[160:163], v187, v187 op_sel_hi:[0,0,0] cbsz:2 blgp:2
	v_mfma_scale_f32_16x16x128_f8f6f4 v[156:159], v[14:19], v[20:25], v[156:159], v187, v187 op_sel_hi:[0,0,0] cbsz:2 blgp:2
	v_mfma_scale_f32_16x16x128_f8f6f4 v[152:155], v[26:31], v[20:25], v[152:155], v187, v187 op_sel_hi:[0,0,0] cbsz:2 blgp:2
	v_mfma_scale_f32_16x16x128_f8f6f4 v[148:151], v[2:7], v[32:37], v[148:151], v187, v187 op_sel_hi:[0,0,0] cbsz:2 blgp:2
	v_mfma_scale_f32_16x16x128_f8f6f4 v[140:143], v[8:13], v[32:37], v[140:143], v187, v187 op_sel_hi:[0,0,0] cbsz:2 blgp:2
	v_mfma_scale_f32_16x16x128_f8f6f4 v[132:135], v[14:19], v[32:37], v[132:135], v187, v187 op_sel_hi:[0,0,0] cbsz:2 blgp:2
	v_mfma_scale_f32_16x16x128_f8f6f4 v[124:127], v[26:31], v[32:37], v[124:127], v187, v187 op_sel_hi:[0,0,0] cbsz:2 blgp:2
	s_setprio 0
	s_cmp_eq_u32 s66, 0
	s_cbranch_scc0 .Lpst2_other
	s_mov_b64 s[38:39], s[2:3]
	s_mov_b32 s40, s11
	s_mov_b32 s41, s35
	s_waitcnt vmcnt(0)
	s_barrier
	s_mov_b32 m0, s60
	s_nop 0
	global_load_lds_dwordx4 v228, s[38:39]
	s_mov_b32 m0, s61
	s_nop 0
	global_load_lds_dwordx4 v229, s[38:39]
	s_mov_b32 m0, s62
	s_nop 0
	global_load_lds_dwordx4 v230, s[38:39]
	s_mov_b32 m0, s63
	s_nop 0
	global_load_lds_dwordx4 v228, s[40:41]
	s_mov_b32 m0, s64
	s_nop 0
	global_load_lds_dwordx4 v229, s[40:41]
	s_mov_b32 m0, s65
	s_nop 0
	global_load_lds_dwordx4 v230, s[40:41]
	s_branch .Lpst2_join

.Lpst2_join:
	s_setprio 1
	s_waitcnt lgkmcnt(0)
	v_mfma_scale_f32_16x16x128_f8f6f4 v[112:115], v[2:7], v[40:45], v[112:115], v187, v187 op_sel_hi:[0,0,0] cbsz:2 blgp:2
	v_mfma_scale_f32_16x16x128_f8f6f4 v[100:103], v[8:13], v[40:45], v[100:103], v187, v187 op_sel_hi:[0,0,0] cbsz:2 blgp:2
	v_mfma_scale_f32_16x16x128_f8f6f4 v[92:95], v[14:19], v[40:45], v[92:95], v187, v187 op_sel_hi:[0,0,0] cbsz:2 blgp:2
	v_mfma_scale_f32_16x16x128_f8f6f4 v[88:91], v[26:31], v[40:45], v[88:91], v187, v187 op_sel_hi:[0,0,0] cbsz:2 blgp:2
	v_mfma_scale_f32_16x16x128_f8f6f4 v[84:87], v[2:7], v[188:193], v[84:87], v187, v187 op_sel_hi:[0,0,0] cbsz:2 blgp:2
	v_mfma_scale_f32_16x16x128_f8f6f4 v[76:79], v[8:13], v[188:193], v[76:79], v187, v187 op_sel_hi:[0,0,0] cbsz:2 blgp:2
	v_mfma_scale_f32_16x16x128_f8f6f4 v[68:71], v[14:19], v[188:193], v[68:71], v187, v187 op_sel_hi:[0,0,0] cbsz:2 blgp:2
	v_mfma_scale_f32_16x16x128_f8f6f4 v[60:63], v[26:31], v[188:193], v[60:63], v187, v187 op_sel_hi:[0,0,0] cbsz:2 blgp:2
	s_setprio 0
	ds_read_b128 v[2:5], v170 offset:12288
	ds_read_b64 v[6:7], v173 offset:12352
	ds_read_b128 v[8:11], v170 offset:13824
	ds_read_b64 v[12:13], v173 offset:13888
	ds_read_b128 v[14:17], v170 offset:15360
	ds_read_b64 v[18:19], v173 offset:15424
	ds_read_b128 v[26:29], v170 offset:16896
	ds_read_b64 v[30:31], v173 offset:16960
	s_setprio 1
	v_mfma_scale_f32_16x16x128_f8f6f4 v[144:147], v[46:51], v[20:25], v[144:147], v187, v187 op_sel_hi:[0,0,0] cbsz:2 blgp:2
	v_mfma_scale_f32_16x16x128_f8f6f4 v[136:139], v[194:199], v[20:25], v[136:139], v187, v187 op_sel_hi:[0,0,0] cbsz:2 blgp:2
	v_mfma_scale_f32_16x16x128_f8f6f4 v[128:131], v[200:205], v[20:25], v[128:131], v187, v187 op_sel_hi:[0,0,0] cbsz:2 blgp:2
	v_mfma_scale_f32_16x16x128_f8f6f4 v[120:123], v[206:211], v[20:25], v[120:123], v187, v187 op_sel_hi:[0,0,0] cbsz:2 blgp:2
	v_mfma_scale_f32_16x16x128_f8f6f4 v[116:119], v[46:51], v[32:37], v[116:119], v187, v187 op_sel_hi:[0,0,0] cbsz:2 blgp:2
	v_mfma_scale_f32_16x16x128_f8f6f4 v[108:111], v[194:199], v[32:37], v[108:111], v187, v187 op_sel_hi:[0,0,0] cbsz:2 blgp:2
	v_mfma_scale_f32_16x16x128_f8f6f4 v[104:107], v[200:205], v[32:37], v[104:107], v187, v187 op_sel_hi:[0,0,0] cbsz:2 blgp:2
	v_mfma_scale_f32_16x16x128_f8f6f4 v[96:99], v[206:211], v[32:37], v[96:99], v187, v187 op_sel_hi:[0,0,0] cbsz:2 blgp:2
	s_setprio 0
	ds_read_b128 v[20:23], v1
	ds_read_b64 v[24:25], v172 offset:64
	ds_read_b128 v[32:35], v1 offset:1536
	ds_read_b64 v[36:37], v172 offset:1600
	s_cmp_eq_u32 s66, 1
	s_cbranch_scc0 .Lpst3_other
	s_add_u32 s38, s2, 0x3000
	s_addc_u32 s39, s3, 0
	s_add_u32 s40, s11, 0x3000
	s_addc_u32 s41, s35, 0
	s_waitcnt vmcnt(0)
	s_barrier
	s_mov_b32 m0, s60
	s_nop 0
	global_load_lds_dwordx4 v228, s[38:39]
	s_mov_b32 m0, s61
	s_nop 0
	global_load_lds_dwordx4 v229, s[38:39]
	s_mov_b32 m0, s62
	s_nop 0
	global_load_lds_dwordx4 v230, s[38:39]
	s_mov_b32 m0, s63
	s_nop 0
	global_load_lds_dwordx4 v228, s[40:41]
	s_mov_b32 m0, s64
	s_nop 0
	global_load_lds_dwordx4 v229, s[40:41]
	s_mov_b32 m0, s65
	s_nop 0
	global_load_lds_dwordx4 v230, s[40:41]
	s_branch .Lpst3_join

.Lpst3_join:
	s_setprio 1
	v_mfma_scale_f32_16x16x128_f8f6f4 v[80:83], v[46:51], v[40:45], v[80:83], v187, v187 op_sel_hi:[0,0,0] cbsz:2 blgp:2
	v_mfma_scale_f32_16x16x128_f8f6f4 v[72:75], v[194:199], v[40:45], v[72:75], v187, v187 op_sel_hi:[0,0,0] cbsz:2 blgp:2
	v_mfma_scale_f32_16x16x128_f8f6f4 v[64:67], v[200:205], v[40:45], v[64:67], v187, v187 op_sel_hi:[0,0,0] cbsz:2 blgp:2
	v_mfma_scale_f32_16x16x128_f8f6f4 v[56:59], v[206:211], v[40:45], v[56:59], v187, v187 op_sel_hi:[0,0,0] cbsz:2 blgp:2
	v_mfma_scale_f32_16x16x128_f8f6f4 v[52:55], v[46:51], v[188:193], v[52:55], v187, v187 op_sel_hi:[0,0,0] cbsz:2 blgp:2
	v_mfma_scale_f32_16x16x128_f8f6f4 v[48:51], v[194:199], v[188:193], v[224:227], v187, v187 op_sel_hi:[0,0,0] cbsz:2 blgp:2
	v_mfma_scale_f32_16x16x128_f8f6f4 v[44:47], v[200:205], v[188:193], v[212:215], v187, v187 op_sel_hi:[0,0,0] cbsz:2 blgp:2
	v_mfma_scale_f32_16x16x128_f8f6f4 v[40:43], v[206:211], v[188:193], v[216:219], v187, v187 op_sel_hi:[0,0,0] cbsz:2 blgp:2
	s_setprio 0
	s_add_i32 s36, s36, 2
	s_add_u32 s11, s11, 0xc000
	s_addc_u32 s35, s35, 0
	s_add_u32 s2, s2, 0xc000
	s_addc_u32 s3, s3, 0
	s_cmp_lt_u32 s36, 4
	s_waitcnt lgkmcnt(0)
.LBB1_3:
	ds_read_b128 v[188:191], v1 offset:24576
	ds_read_b64 v[192:193], v172 offset:24640
	ds_read_b128 v[194:197], v1 offset:26112
	ds_read_b64 v[198:199], v172 offset:26176
	ds_read_b128 v[200:203], v170 offset:36864
	ds_read_b64 v[204:205], v173 offset:36928
	ds_read_b128 v[206:209], v170 offset:38400
	ds_read_b64 v[210:211], v173 offset:38464
	ds_read_b128 v[212:215], v170 offset:39936
	ds_read_b64 v[216:217], v173 offset:40000
	ds_read_b128 v[218:221], v170 offset:41472
	ds_read_b64 v[222:223], v173 offset:41536
	s_setprio 1
	v_mfma_scale_f32_16x16x128_f8f6f4 v[164:167], v[2:7], v[20:25], v[164:167], v187, v187 op_sel_hi:[0,0,0] cbsz:2 blgp:2
	v_mfma_scale_f32_16x16x128_f8f6f4 v[160:163], v[8:13], v[20:25], v[160:163], v187, v187 op_sel_hi:[0,0,0] cbsz:2 blgp:2
	v_mfma_scale_f32_16x16x128_f8f6f4 v[156:159], v[14:19], v[20:25], v[156:159], v187, v187 op_sel_hi:[0,0,0] cbsz:2 blgp:2
	v_mfma_scale_f32_16x16x128_f8f6f4 v[152:155], v[26:31], v[20:25], v[152:155], v187, v187 op_sel_hi:[0,0,0] cbsz:2 blgp:2
	v_mfma_scale_f32_16x16x128_f8f6f4 v[148:151], v[2:7], v[32:37], v[148:151], v187, v187 op_sel_hi:[0,0,0] cbsz:2 blgp:2
	v_mfma_scale_f32_16x16x128_f8f6f4 v[140:143], v[8:13], v[32:37], v[140:143], v187, v187 op_sel_hi:[0,0,0] cbsz:2 blgp:2
	v_mfma_scale_f32_16x16x128_f8f6f4 v[132:135], v[14:19], v[32:37], v[132:135], v187, v187 op_sel_hi:[0,0,0] cbsz:2 blgp:2
	v_mfma_scale_f32_16x16x128_f8f6f4 v[124:127], v[26:31], v[32:37], v[124:127], v187, v187 op_sel_hi:[0,0,0] cbsz:2 blgp:2
	s_setprio 0
	s_cmp_eq_u32 s66, 0
	s_cbranch_scc0 .Lst0_other
	s_add_u32 s38, s2, 0xffffa000
	s_addc_u32 s39, s3, -1
	s_add_u32 s40, s11, 0xffffa000
	s_addc_u32 s41, s35, -1
	s_waitcnt vmcnt(0)
	s_barrier
	s_mov_b32 m0, s54
	s_nop 0
	global_load_lds_dwordx4 v228, s[38:39]
	s_mov_b32 m0, s55
	s_nop 0
	global_load_lds_dwordx4 v229, s[38:39]
	s_mov_b32 m0, s56
	s_nop 0
	global_load_lds_dwordx4 v230, s[38:39]
	s_mov_b32 m0, s57
	s_nop 0
	global_load_lds_dwordx4 v228, s[40:41]
	s_mov_b32 m0, s58
	s_nop 0
	global_load_lds_dwordx4 v229, s[40:41]
	s_mov_b32 m0, s59
	s_nop 0
	global_load_lds_dwordx4 v230, s[40:41]
	s_branch .Lst0_join

.Lst0_join:
	s_setprio 1
	s_waitcnt lgkmcnt(0)
	v_mfma_scale_f32_16x16x128_f8f6f4 v[112:115], v[2:7], v[188:193], v[112:115], v187, v187 op_sel_hi:[0,0,0] cbsz:2 blgp:2
	v_mfma_scale_f32_16x16x128_f8f6f4 v[100:103], v[8:13], v[188:193], v[100:103], v187, v187 op_sel_hi:[0,0,0] cbsz:2 blgp:2
	v_mfma_scale_f32_16x16x128_f8f6f4 v[92:95], v[14:19], v[188:193], v[92:95], v187, v187 op_sel_hi:[0,0,0] cbsz:2 blgp:2
	v_mfma_scale_f32_16x16x128_f8f6f4 v[88:91], v[26:31], v[188:193], v[88:91], v187, v187 op_sel_hi:[0,0,0] cbsz:2 blgp:2
	v_mfma_scale_f32_16x16x128_f8f6f4 v[84:87], v[2:7], v[194:199], v[84:87], v187, v187 op_sel_hi:[0,0,0] cbsz:2 blgp:2
	v_mfma_scale_f32_16x16x128_f8f6f4 v[76:79], v[8:13], v[194:199], v[76:79], v187, v187 op_sel_hi:[0,0,0] cbsz:2 blgp:2
	v_mfma_scale_f32_16x16x128_f8f6f4 v[68:71], v[14:19], v[194:199], v[68:71], v187, v187 op_sel_hi:[0,0,0] cbsz:2 blgp:2
	v_mfma_scale_f32_16x16x128_f8f6f4 v[60:63], v[26:31], v[194:199], v[60:63], v187, v187 op_sel_hi:[0,0,0] cbsz:2 blgp:2
	s_setprio 0
	ds_read_b128 v[2:5], v170 offset:61440
	ds_read_b64 v[6:7], v173 offset:61504
	ds_read_b128 v[8:11], v170 offset:62976
	ds_read_b64 v[12:13], v173 offset:63040
	ds_read_b128 v[14:17], v170 offset:64512
	ds_read_b64 v[18:19], v173 offset:64576
	ds_read_b128 v[26:29], v171 offset:53760
	ds_read_b64 v[30:31], v174 offset:53760
	s_setprio 1
	v_mfma_scale_f32_16x16x128_f8f6f4 v[144:147], v[200:205], v[20:25], v[144:147], v187, v187 op_sel_hi:[0,0,0] cbsz:2 blgp:2
	v_mfma_scale_f32_16x16x128_f8f6f4 v[136:139], v[206:211], v[20:25], v[136:139], v187, v187 op_sel_hi:[0,0,0] cbsz:2 blgp:2
	v_mfma_scale_f32_16x16x128_f8f6f4 v[128:131], v[212:217], v[20:25], v[128:131], v187, v187 op_sel_hi:[0,0,0] cbsz:2 blgp:2
	v_mfma_scale_f32_16x16x128_f8f6f4 v[120:123], v[218:223], v[20:25], v[120:123], v187, v187 op_sel_hi:[0,0,0] cbsz:2 blgp:2
	v_mfma_scale_f32_16x16x128_f8f6f4 v[116:119], v[200:205], v[32:37], v[116:119], v187, v187 op_sel_hi:[0,0,0] cbsz:2 blgp:2
	v_mfma_scale_f32_16x16x128_f8f6f4 v[108:111], v[206:211], v[32:37], v[108:111], v187, v187 op_sel_hi:[0,0,0] cbsz:2 blgp:2
	v_mfma_scale_f32_16x16x128_f8f6f4 v[104:107], v[212:217], v[32:37], v[104:107], v187, v187 op_sel_hi:[0,0,0] cbsz:2 blgp:2
	v_mfma_scale_f32_16x16x128_f8f6f4 v[96:99], v[218:223], v[32:37], v[96:99], v187, v187 op_sel_hi:[0,0,0] cbsz:2 blgp:2
	s_setprio 0
	ds_read_b128 v[20:23], v1 offset:49152
	ds_read_b64 v[24:25], v172 offset:49216
	ds_read_b128 v[32:35], v1 offset:50688
	ds_read_b64 v[36:37], v172 offset:50752
	s_cmp_eq_u32 s66, 1
	s_cbranch_scc0 .Lst1_other
	s_add_u32 s38, s2, 0xffffd000
	s_addc_u32 s39, s3, -1
	s_add_u32 s40, s11, 0xffffd000
	s_addc_u32 s41, s35, -1
	s_waitcnt vmcnt(0)
	s_barrier
	s_mov_b32 m0, s54
	s_nop 0
	global_load_lds_dwordx4 v228, s[38:39]
	s_mov_b32 m0, s55
	s_nop 0
	global_load_lds_dwordx4 v229, s[38:39]
	s_mov_b32 m0, s56
	s_nop 0
	global_load_lds_dwordx4 v230, s[38:39]
	s_mov_b32 m0, s57
	s_nop 0
	global_load_lds_dwordx4 v228, s[40:41]
	s_mov_b32 m0, s58
	s_nop 0
	global_load_lds_dwordx4 v229, s[40:41]
	s_mov_b32 m0, s59
	s_nop 0
	global_load_lds_dwordx4 v230, s[40:41]
	s_branch .Lst1_join

.Lst1_join:
	s_setprio 1
	v_mfma_scale_f32_16x16x128_f8f6f4 v[80:83], v[200:205], v[188:193], v[80:83], v187, v187 op_sel_hi:[0,0,0] cbsz:2 blgp:2
	v_mfma_scale_f32_16x16x128_f8f6f4 v[72:75], v[206:211], v[188:193], v[72:75], v187, v187 op_sel_hi:[0,0,0] cbsz:2 blgp:2
	v_mfma_scale_f32_16x16x128_f8f6f4 v[64:67], v[212:217], v[188:193], v[64:67], v187, v187 op_sel_hi:[0,0,0] cbsz:2 blgp:2
	v_mfma_scale_f32_16x16x128_f8f6f4 v[56:59], v[218:223], v[188:193], v[56:59], v187, v187 op_sel_hi:[0,0,0] cbsz:2 blgp:2
	v_mfma_scale_f32_16x16x128_f8f6f4 v[52:55], v[200:205], v[194:199], v[52:55], v187, v187 op_sel_hi:[0,0,0] cbsz:2 blgp:2
	v_mfma_scale_f32_16x16x128_f8f6f4 v[224:227], v[206:211], v[194:199], v[48:51], v187, v187 op_sel_hi:[0,0,0] cbsz:2 blgp:2
	v_mfma_scale_f32_16x16x128_f8f6f4 v[212:215], v[212:217], v[194:199], v[44:47], v187, v187 op_sel_hi:[0,0,0] cbsz:2 blgp:2
	v_mfma_scale_f32_16x16x128_f8f6f4 v[216:219], v[218:223], v[194:199], v[40:43], v187, v187 op_sel_hi:[0,0,0] cbsz:2 blgp:2
	s_setprio 0
	s_waitcnt lgkmcnt(0)
	s_nop 0
	ds_read_b128 v[40:43], v175
	ds_read_b64 v[44:45], v176
	ds_read_b128 v[188:191], v179
	ds_read_b64 v[192:193], v180
	ds_read_b128 v[46:49], v177
	ds_read_b64 v[50:51], v178
	ds_read_b128 v[194:197], v181
	ds_read_b64 v[198:199], v182
	ds_read_b128 v[200:203], v183
	ds_read_b64 v[204:205], v184
	ds_read_b128 v[206:209], v185
	ds_read_b64 v[210:211], v186
	s_setprio 1
	v_mfma_scale_f32_16x16x128_f8f6f4 v[164:167], v[2:7], v[20:25], v[164:167], v187, v187 op_sel_hi:[0,0,0] cbsz:2 blgp:2
	v_mfma_scale_f32_16x16x128_f8f6f4 v[160:163], v[8:13], v[20:25], v[160:163], v187, v187 op_sel_hi:[0,0,0] cbsz:2 blgp:2
	v_mfma_scale_f32_16x16x128_f8f6f4 v[156:159], v[14:19], v[20:25], v[156:159], v187, v187 op_sel_hi:[0,0,0] cbsz:2 blgp:2
	v_mfma_scale_f32_16x16x128_f8f6f4 v[152:155], v[26:31], v[20:25], v[152:155], v187, v187 op_sel_hi:[0,0,0] cbsz:2 blgp:2
	v_mfma_scale_f32_16x16x128_f8f6f4 v[148:151], v[2:7], v[32:37], v[148:151], v187, v187 op_sel_hi:[0,0,0] cbsz:2 blgp:2
	v_mfma_scale_f32_16x16x128_f8f6f4 v[140:143], v[8:13], v[32:37], v[140:143], v187, v187 op_sel_hi:[0,0,0] cbsz:2 blgp:2
	v_mfma_scale_f32_16x16x128_f8f6f4 v[132:135], v[14:19], v[32:37], v[132:135], v187, v187 op_sel_hi:[0,0,0] cbsz:2 blgp:2
	v_mfma_scale_f32_16x16x128_f8f6f4 v[124:127], v[26:31], v[32:37], v[124:127], v187, v187 op_sel_hi:[0,0,0] cbsz:2 blgp:2
	s_setprio 0
	s_cmp_eq_u32 s66, 0
	s_cbranch_scc0 .Lst2_other
	s_mov_b64 s[38:39], s[2:3]
	s_mov_b32 s40, s11
	s_mov_b32 s41, s35
	s_waitcnt vmcnt(0)
	s_barrier
	s_mov_b32 m0, s60
	s_nop 0
	global_load_lds_dwordx4 v228, s[38:39]
	s_mov_b32 m0, s61
	s_nop 0
	global_load_lds_dwordx4 v229, s[38:39]
	s_mov_b32 m0, s62
	s_nop 0
	global_load_lds_dwordx4 v230, s[38:39]
	s_mov_b32 m0, s63
	s_nop 0
	global_load_lds_dwordx4 v228, s[40:41]
	s_mov_b32 m0, s64
	s_nop 0
	global_load_lds_dwordx4 v229, s[40:41]
	s_mov_b32 m0, s65
	s_nop 0
	global_load_lds_dwordx4 v230, s[40:41]
	s_branch .Lst2_join

.Lst3_join:
	s_setprio 1
	v_mfma_scale_f32_16x16x128_f8f6f4 v[80:83], v[46:51], v[40:45], v[80:83], v187, v187 op_sel_hi:[0,0,0] cbsz:2 blgp:2
	v_mfma_scale_f32_16x16x128_f8f6f4 v[72:75], v[194:199], v[40:45], v[72:75], v187, v187 op_sel_hi:[0,0,0] cbsz:2 blgp:2
	v_mfma_scale_f32_16x16x128_f8f6f4 v[64:67], v[200:205], v[40:45], v[64:67], v187, v187 op_sel_hi:[0,0,0] cbsz:2 blgp:2
	v_mfma_scale_f32_16x16x128_f8f6f4 v[56:59], v[206:211], v[40:45], v[56:59], v187, v187 op_sel_hi:[0,0,0] cbsz:2 blgp:2
	v_mfma_scale_f32_16x16x128_f8f6f4 v[52:55], v[46:51], v[188:193], v[52:55], v187, v187 op_sel_hi:[0,0,0] cbsz:2 blgp:2
	v_mfma_scale_f32_16x16x128_f8f6f4 v[48:51], v[194:199], v[188:193], v[224:227], v187, v187 op_sel_hi:[0,0,0] cbsz:2 blgp:2
	v_mfma_scale_f32_16x16x128_f8f6f4 v[44:47], v[200:205], v[188:193], v[212:215], v187, v187 op_sel_hi:[0,0,0] cbsz:2 blgp:2
	v_mfma_scale_f32_16x16x128_f8f6f4 v[40:43], v[206:211], v[188:193], v[216:219], v187, v187 op_sel_hi:[0,0,0] cbsz:2 blgp:2
	s_setprio 0
	s_add_i32 s36, s36, 2
	s_add_u32 s11, s11, 0xc000
	s_addc_u32 s35, s35, 0
	s_add_u32 s2, s2, 0xc000
	s_addc_u32 s3, s3, 0
	s_cmp_lt_u32 s36, 4
	s_waitcnt lgkmcnt(0)
	s_cbranch_scc1 .LBB1_3
	s_mov_b32 s2, 1
	s_cmp_lt_i32 s2, 1
	s_cbranch_scc1 .LBB1_6
.LBB1_5:
	ds_read_b128 v[188:191], v1 offset:24576
	ds_read_b64 v[192:193], v172 offset:24640
	ds_read_b128 v[194:197], v1 offset:26112
	ds_read_b64 v[198:199], v172 offset:26176
	ds_read_b128 v[200:203], v170 offset:36864
	ds_read_b64 v[204:205], v173 offset:36928
	ds_read_b128 v[206:209], v170 offset:38400
	ds_read_b64 v[210:211], v173 offset:38464
	ds_read_b128 v[212:215], v170 offset:39936
	ds_read_b64 v[216:217], v173 offset:40000
	ds_read_b128 v[218:221], v170 offset:41472
	ds_read_b64 v[222:223], v173 offset:41536
	s_setprio 1
	v_mfma_scale_f32_16x16x128_f8f6f4 v[164:167], v[2:7], v[20:25], v[164:167], v187, v187 op_sel_hi:[0,0,0] cbsz:2 blgp:2
	v_mfma_scale_f32_16x16x128_f8f6f4 v[160:163], v[8:13], v[20:25], v[160:163], v187, v187 op_sel_hi:[0,0,0] cbsz:2 blgp:2
	v_mfma_scale_f32_16x16x128_f8f6f4 v[156:159], v[14:19], v[20:25], v[156:159], v187, v187 op_sel_hi:[0,0,0] cbsz:2 blgp:2
	v_mfma_scale_f32_16x16x128_f8f6f4 v[152:155], v[26:31], v[20:25], v[152:155], v187, v187 op_sel_hi:[0,0,0] cbsz:2 blgp:2
	v_mfma_scale_f32_16x16x128_f8f6f4 v[148:151], v[2:7], v[32:37], v[148:151], v187, v187 op_sel_hi:[0,0,0] cbsz:2 blgp:2
	v_mfma_scale_f32_16x16x128_f8f6f4 v[140:143], v[8:13], v[32:37], v[140:143], v187, v187 op_sel_hi:[0,0,0] cbsz:2 blgp:2
	v_mfma_scale_f32_16x16x128_f8f6f4 v[132:135], v[14:19], v[32:37], v[132:135], v187, v187 op_sel_hi:[0,0,0] cbsz:2 blgp:2
	v_mfma_scale_f32_16x16x128_f8f6f4 v[124:127], v[26:31], v[32:37], v[124:127], v187, v187 op_sel_hi:[0,0,0] cbsz:2 blgp:2
	s_setprio 0
	s_cmp_eq_u32 s66, 0
	s_cbranch_scc0 .Ltail_nowait
	s_waitcnt vmcnt(0)
.Ltail_nowait:
	s_barrier
	s_setprio 1
	s_waitcnt lgkmcnt(0)
	v_mfma_scale_f32_16x16x128_f8f6f4 v[112:115], v[2:7], v[188:193], v[112:115], v187, v187 op_sel_hi:[0,0,0] cbsz:2 blgp:2
	v_mfma_scale_f32_16x16x128_f8f6f4 v[100:103], v[8:13], v[188:193], v[100:103], v187, v187 op_sel_hi:[0,0,0] cbsz:2 blgp:2
	v_mfma_scale_f32_16x16x128_f8f6f4 v[92:95], v[14:19], v[188:193], v[92:95], v187, v187 op_sel_hi:[0,0,0] cbsz:2 blgp:2
	v_mfma_scale_f32_16x16x128_f8f6f4 v[88:91], v[26:31], v[188:193], v[88:91], v187, v187 op_sel_hi:[0,0,0] cbsz:2 blgp:2
	v_mfma_scale_f32_16x16x128_f8f6f4 v[84:87], v[2:7], v[194:199], v[84:87], v187, v187 op_sel_hi:[0,0,0] cbsz:2 blgp:2
	v_mfma_scale_f32_16x16x128_f8f6f4 v[76:79], v[8:13], v[194:199], v[76:79], v187, v187 op_sel_hi:[0,0,0] cbsz:2 blgp:2
	v_mfma_scale_f32_16x16x128_f8f6f4 v[68:71], v[14:19], v[194:199], v[68:71], v187, v187 op_sel_hi:[0,0,0] cbsz:2 blgp:2
	v_mfma_scale_f32_16x16x128_f8f6f4 v[60:63], v[26:31], v[194:199], v[60:63], v187, v187 op_sel_hi:[0,0,0] cbsz:2 blgp:2
	s_setprio 0
	ds_read_b128 v[2:5], v170 offset:61440
	ds_read_b64 v[6:7], v173 offset:61504
	ds_read_b128 v[8:11], v170 offset:62976
	ds_read_b64 v[12:13], v173 offset:63040
	ds_read_b128 v[14:17], v170 offset:64512
	ds_read_b64 v[18:19], v173 offset:64576
	ds_read_b128 v[26:29], v171 offset:53760
	ds_read_b64 v[30:31], v174 offset:53760
	s_setprio 1
	v_mfma_scale_f32_16x16x128_f8f6f4 v[144:147], v[200:205], v[20:25], v[144:147], v187, v187 op_sel_hi:[0,0,0] cbsz:2 blgp:2
	v_mfma_scale_f32_16x16x128_f8f6f4 v[136:139], v[206:211], v[20:25], v[136:139], v187, v187 op_sel_hi:[0,0,0] cbsz:2 blgp:2
	v_mfma_scale_f32_16x16x128_f8f6f4 v[128:131], v[212:217], v[20:25], v[128:131], v187, v187 op_sel_hi:[0,0,0] cbsz:2 blgp:2
	v_mfma_scale_f32_16x16x128_f8f6f4 v[120:123], v[218:223], v[20:25], v[120:123], v187, v187 op_sel_hi:[0,0,0] cbsz:2 blgp:2
	v_mfma_scale_f32_16x16x128_f8f6f4 v[116:119], v[200:205], v[32:37], v[116:119], v187, v187 op_sel_hi:[0,0,0] cbsz:2 blgp:2
	v_mfma_scale_f32_16x16x128_f8f6f4 v[108:111], v[206:211], v[32:37], v[108:111], v187, v187 op_sel_hi:[0,0,0] cbsz:2 blgp:2
	v_mfma_scale_f32_16x16x128_f8f6f4 v[104:107], v[212:217], v[32:37], v[104:107], v187, v187 op_sel_hi:[0,0,0] cbsz:2 blgp:2
	v_mfma_scale_f32_16x16x128_f8f6f4 v[96:99], v[218:223], v[32:37], v[96:99], v187, v187 op_sel_hi:[0,0,0] cbsz:2 blgp:2
	s_setprio 0
	ds_read_b128 v[20:23], v1 offset:49152
	ds_read_b64 v[24:25], v172 offset:49216
	ds_read_b128 v[32:35], v1 offset:50688
	ds_read_b64 v[36:37], v172 offset:50752
	s_waitcnt vmcnt(0)
	s_barrier
	s_setprio 1
	v_mfma_scale_f32_16x16x128_f8f6f4 v[80:83], v[200:205], v[188:193], v[80:83], v187, v187 op_sel_hi:[0,0,0] cbsz:2 blgp:2
	v_mfma_scale_f32_16x16x128_f8f6f4 v[72:75], v[206:211], v[188:193], v[72:75], v187, v187 op_sel_hi:[0,0,0] cbsz:2 blgp:2
	v_mfma_scale_f32_16x16x128_f8f6f4 v[64:67], v[212:217], v[188:193], v[64:67], v187, v187 op_sel_hi:[0,0,0] cbsz:2 blgp:2
	v_mfma_scale_f32_16x16x128_f8f6f4 v[56:59], v[218:223], v[188:193], v[56:59], v187, v187 op_sel_hi:[0,0,0] cbsz:2 blgp:2
	v_mfma_scale_f32_16x16x128_f8f6f4 v[52:55], v[200:205], v[194:199], v[52:55], v187, v187 op_sel_hi:[0,0,0] cbsz:2 blgp:2
	v_mfma_scale_f32_16x16x128_f8f6f4 v[224:227], v[206:211], v[194:199], v[48:51], v187, v187 op_sel_hi:[0,0,0] cbsz:2 blgp:2
	v_mfma_scale_f32_16x16x128_f8f6f4 v[212:215], v[212:217], v[194:199], v[44:47], v187, v187 op_sel_hi:[0,0,0] cbsz:2 blgp:2
	v_mfma_scale_f32_16x16x128_f8f6f4 v[216:219], v[218:223], v[194:199], v[40:43], v187, v187 op_sel_hi:[0,0,0] cbsz:2 blgp:2
	s_setprio 0
	s_waitcnt lgkmcnt(0)
	s_nop 0
	ds_read_b128 v[40:43], v175
	ds_read_b64 v[44:45], v176
	ds_read_b128 v[188:191], v179
	ds_read_b64 v[192:193], v180
	ds_read_b128 v[46:49], v177
	ds_read_b64 v[50:51], v178
	ds_read_b128 v[194:197], v181
	ds_read_b64 v[198:199], v182
	ds_read_b128 v[200:203], v183
	ds_read_b64 v[204:205], v184
	ds_read_b128 v[206:209], v185
	ds_read_b64 v[210:211], v186
	s_setprio 1
	v_mfma_scale_f32_16x16x128_f8f6f4 v[164:167], v[2:7], v[20:25], v[164:167], v187, v187 op_sel_hi:[0,0,0] cbsz:2 blgp:2
	v_mfma_scale_f32_16x16x128_f8f6f4 v[160:163], v[8:13], v[20:25], v[160:163], v187, v187 op_sel_hi:[0,0,0] cbsz:2 blgp:2
	v_mfma_scale_f32_16x16x128_f8f6f4 v[156:159], v[14:19], v[20:25], v[156:159], v187, v187 op_sel_hi:[0,0,0] cbsz:2 blgp:2
	v_mfma_scale_f32_16x16x128_f8f6f4 v[152:155], v[26:31], v[20:25], v[152:155], v187, v187 op_sel_hi:[0,0,0] cbsz:2 blgp:2
	v_mfma_scale_f32_16x16x128_f8f6f4 v[148:151], v[2:7], v[32:37], v[148:151], v187, v187 op_sel_hi:[0,0,0] cbsz:2 blgp:2
	v_mfma_scale_f32_16x16x128_f8f6f4 v[140:143], v[8:13], v[32:37], v[140:143], v187, v187 op_sel_hi:[0,0,0] cbsz:2 blgp:2
	v_mfma_scale_f32_16x16x128_f8f6f4 v[132:135], v[14:19], v[32:37], v[132:135], v187, v187 op_sel_hi:[0,0,0] cbsz:2 blgp:2
	v_mfma_scale_f32_16x16x128_f8f6f4 v[124:127], v[26:31], v[32:37], v[124:127], v187, v187 op_sel_hi:[0,0,0] cbsz:2 blgp:2
	s_setprio 0
	s_setprio 1
	s_waitcnt lgkmcnt(0)
	v_mfma_scale_f32_16x16x128_f8f6f4 v[112:115], v[2:7], v[40:45], v[112:115], v187, v187 op_sel_hi:[0,0,0] cbsz:2 blgp:2
	v_mfma_scale_f32_16x16x128_f8f6f4 v[100:103], v[8:13], v[40:45], v[100:103], v187, v187 op_sel_hi:[0,0,0] cbsz:2 blgp:2
	v_mfma_scale_f32_16x16x128_f8f6f4 v[92:95], v[14:19], v[40:45], v[92:95], v187, v187 op_sel_hi:[0,0,0] cbsz:2 blgp:2
	v_mfma_scale_f32_16x16x128_f8f6f4 v[88:91], v[26:31], v[40:45], v[88:91], v187, v187 op_sel_hi:[0,0,0] cbsz:2 blgp:2
	v_mfma_scale_f32_16x16x128_f8f6f4 v[84:87], v[2:7], v[188:193], v[84:87], v187, v187 op_sel_hi:[0,0,0] cbsz:2 blgp:2
	v_mfma_scale_f32_16x16x128_f8f6f4 v[76:79], v[8:13], v[188:193], v[76:79], v187, v187 op_sel_hi:[0,0,0] cbsz:2 blgp:2
	v_mfma_scale_f32_16x16x128_f8f6f4 v[68:71], v[14:19], v[188:193], v[68:71], v187, v187 op_sel_hi:[0,0,0] cbsz:2 blgp:2
	v_mfma_scale_f32_16x16x128_f8f6f4 v[60:63], v[26:31], v[188:193], v[60:63], v187, v187 op_sel_hi:[0,0,0] cbsz:2 blgp:2
	s_setprio 0
	s_setprio 1
	v_mfma_scale_f32_16x16x128_f8f6f4 v[144:147], v[46:51], v[20:25], v[144:147], v187, v187 op_sel_hi:[0,0,0] cbsz:2 blgp:2
	v_mfma_scale_f32_16x16x128_f8f6f4 v[136:139], v[194:199], v[20:25], v[136:139], v187, v187 op_sel_hi:[0,0,0] cbsz:2 blgp:2
	v_mfma_scale_f32_16x16x128_f8f6f4 v[128:131], v[200:205], v[20:25], v[128:131], v187, v187 op_sel_hi:[0,0,0] cbsz:2 blgp:2
	v_mfma_scale_f32_16x16x128_f8f6f4 v[120:123], v[206:211], v[20:25], v[120:123], v187, v187 op_sel_hi:[0,0,0] cbsz:2 blgp:2
	v_mfma_scale_f32_16x16x128_f8f6f4 v[116:119], v[46:51], v[32:37], v[116:119], v187, v187 op_sel_hi:[0,0,0] cbsz:2 blgp:2
	v_mfma_scale_f32_16x16x128_f8f6f4 v[108:111], v[194:199], v[32:37], v[108:111], v187, v187 op_sel_hi:[0,0,0] cbsz:2 blgp:2
	v_mfma_scale_f32_16x16x128_f8f6f4 v[104:107], v[200:205], v[32:37], v[104:107], v187, v187 op_sel_hi:[0,0,0] cbsz:2 blgp:2
	v_mfma_scale_f32_16x16x128_f8f6f4 v[96:99], v[206:211], v[32:37], v[96:99], v187, v187 op_sel_hi:[0,0,0] cbsz:2 blgp:2
	s_setprio 0
	s_setprio 1
	v_mfma_scale_f32_16x16x128_f8f6f4 v[80:83], v[46:51], v[40:45], v[80:83], v187, v187 op_sel_hi:[0,0,0] cbsz:2 blgp:2
	v_mfma_scale_f32_16x16x128_f8f6f4 v[72:75], v[194:199], v[40:45], v[72:75], v187, v187 op_sel_hi:[0,0,0] cbsz:2 blgp:2
	v_mfma_scale_f32_16x16x128_f8f6f4 v[64:67], v[200:205], v[40:45], v[64:67], v187, v187 op_sel_hi:[0,0,0] cbsz:2 blgp:2
	v_mfma_scale_f32_16x16x128_f8f6f4 v[56:59], v[206:211], v[40:45], v[56:59], v187, v187 op_sel_hi:[0,0,0] cbsz:2 blgp:2
	v_mfma_scale_f32_16x16x128_f8f6f4 v[52:55], v[46:51], v[188:193], v[52:55], v187, v187 op_sel_hi:[0,0,0] cbsz:2 blgp:2
	v_mfma_scale_f32_16x16x128_f8f6f4 v[48:51], v[194:199], v[188:193], v[224:227], v187, v187 op_sel_hi:[0,0,0] cbsz:2 blgp:2
	v_mfma_scale_f32_16x16x128_f8f6f4 v[44:47], v[200:205], v[188:193], v[212:215], v187, v187 op_sel_hi:[0,0,0] cbsz:2 blgp:2
	v_mfma_scale_f32_16x16x128_f8f6f4 v[40:43], v[206:211], v[188:193], v[216:219], v187, v187 op_sel_hi:[0,0,0] cbsz:2 blgp:2
	s_setprio 0
	s_add_i32 s2, s2, -1
	s_cmp_lg_u32 s2, 0
	s_cbranch_scc1 .LBB1_5
.LBB1_6:
	s_add_i32 s2, s10, 0x100
	s_cmpk_gt_i32 s10, 0xb37
	s_cselect_b64 s[10:11], -1, 0
	s_and_b64 vcc, exec, s[10:11]
	s_mov_b32 s3, s13
	s_mov_b32 s35, s34
	s_cbranch_vccnz .LBB1_1
	s_ashr_i32 s3, s2, 31
	s_lshr_b32 s3, s3, 29
	s_add_i32 s3, s2, s3
	s_ashr_i32 s35, s3, 3
	s_and_b32 s3, s3, -8
	s_sub_i32 s3, s2, s3
	s_cmp_lt_i32 s3, 0
	s_cselect_b32 s36, s12, 0x187
	s_mul_i32 s3, s36, s3
	s_add_i32 s3, s3, s35
	s_ashr_i32 s35, s3, 31
	s_lshr_b32 s35, s35, 27
	s_add_i32 s35, s3, s35
	s_ashr_i32 s36, s35, 5
	s_lshl_b32 s38, s36, 2
	s_sub_i32 s36, 0x187, s38
	s_min_u32 s39, s36, 4
	s_andn2_b32 s35, s35, 31
	s_sub_i32 s3, s3, s35
	v_cvt_f32_ubyte0_e32 v3, s39
	v_cvt_f32_i32_e32 v2, s3
	v_rcp_iflag_f32_e32 v4, v3
	s_ashr_i32 s35, s3, 30
	s_or_b32 s35, s35, 1
	v_mul_f32_e32 v4, v2, v4
	v_trunc_f32_e32 v4, v4
	v_fma_f32 v2, -v4, v3, v2
	v_cvt_i32_f32_e32 v4, v4
	v_cmp_ge_f32_e64 s[36:37], |v2|, v3
	s_and_b64 s[36:37], s[36:37], exec
	s_cselect_b32 s35, s35, 0
	v_readfirstlane_b32 s36, v4
	s_add_i32 s36, s36, s35
	s_mul_i32 s35, s36, s39
	s_sub_i32 s3, s35, s3
	s_sext_i32_i8 s3, s3
	s_sub_i32 s3, s3, s38
	s_bfe_i64 s[38:39], s[36:37], 0x80000
	s_addk_i32 s3, 0x186
	s_mul_i32 s37, s38, 0x30000
	s_mul_hi_i32 s35, s38, 0x30000
	s_add_u32 s38, s6, s37
	s_addc_u32 s39, s7, s35
	s_mul_i32 s37, s3, 0x30000
	s_mul_hi_i32 s35, s3, 0x30000
	s_add_u32 s37, s4, s37
	s_addc_u32 s35, s5, s35
	s_add_u32 s42, s38, 0x2000
	s_addc_u32 s43, s39, 0
	s_add_u32 s44, s37, 0xfffff000
	s_addc_u32 s45, s35, -1
	s_and_b64 s[40:41], s[0:1], exec
	s_cselect_b32 s41, s43, s45
	s_cselect_b32 s40, s42, s44
	s_add_u32 s42, s37, 0x1000
	s_addc_u32 s43, s35, 0
	s_mov_b64 s[44:45], s[38:39]
	s_nop 0
	s_add_u32 s40, s38, 0x3000
	s_addc_u32 s41, s39, 0
	s_add_u32 s42, s38, 0x5000
	s_addc_u32 s43, s39, 0
	s_add_u32 s44, s37, 0x2000
	s_addc_u32 s45, s35, 0
	s_and_b64 s[38:39], s[0:1], exec
	s_cselect_b32 s39, s43, s45
	s_cselect_b32 s38, s42, s44
	s_add_u32 s42, s37, 0x4000
	s_addc_u32 s43, s35, 0
	s_sext_i32_i8 s35, s36
	s_nop 0
	s_mul_i32 s68, s35, 0x30000
	s_mul_hi_i32 s69, s35, 0x30000
	s_add_u32 s68, s6, s68
	s_addc_u32 s69, s7, s69
	s_mul_i32 s70, s3, 0x30000
	s_mul_hi_i32 s71, s3, 0x30000
	s_add_u32 s70, s4, s70
	s_addc_u32 s71, s5, s71
	s_mul_i32 s67, s66, 0x3000
	s_add_u32 s68, s68, s67
	s_addc_u32 s69, s69, 0
	s_add_u32 s70, s70, s67
	s_addc_u32 s71, s71, 0
	s_mov_b32 m0, s54
	s_nop 0
	global_load_lds_dwordx4 v228, s[68:69]
	s_mov_b32 m0, s55
	s_nop 0
	global_load_lds_dwordx4 v229, s[68:69]
	s_mov_b32 m0, s56
	s_nop 0
	global_load_lds_dwordx4 v230, s[68:69]
	s_mov_b32 m0, s57
	s_nop 0
	global_load_lds_dwordx4 v228, s[70:71]
	s_mov_b32 m0, s58
	s_nop 0
	global_load_lds_dwordx4 v229, s[70:71]
	s_mov_b32 m0, s59
	s_nop 0
	global_load_lds_dwordx4 v230, s[70:71]
	s_branch .LBB1_1

	.amdhsa_kernel _Z8knn_gemmPKcS0_Pi
		.amdhsa_group_segment_fixed_size 0
		.amdhsa_private_segment_fixed_size 0
		.amdhsa_kernarg_size 24
		.amdhsa_user_sgpr_count 2
		.amdhsa_user_sgpr_dispatch_ptr 0
		.amdhsa_user_sgpr_queue_ptr 0
		.amdhsa_user_sgpr_kernarg_segment_ptr 1
		.amdhsa_user_sgpr_dispatch_id 0
		.amdhsa_user_sgpr_kernarg_preload_length 0
		.amdhsa_user_sgpr_kernarg_preload_offset 0
		.amdhsa_user_sgpr_private_segment_size 0
		.amdhsa_uses_dynamic_stack 0
		.amdhsa_enable_private_segment 0
		.amdhsa_system_sgpr_workgroup_id_x 1
		.amdhsa_system_sgpr_workgroup_id_y 0
		.amdhsa_system_sgpr_workgroup_id_z 0
		.amdhsa_system_sgpr_workgroup_info 0
		.amdhsa_system_vgpr_workitem_id 0
		.amdhsa_next_free_vgpr 232
		.amdhsa_next_free_sgpr 72
		.amdhsa_accum_offset 232
		.amdhsa_reserve_vcc 1
		.amdhsa_float_round_mode_32 0
		.amdhsa_float_round_mode_16_64 0
		.amdhsa_float_denorm_mode_32 3
		.amdhsa_float_denorm_mode_16_64 3
		.amdhsa_dx10_clamp 1
		.amdhsa_ieee_mode 1
		.amdhsa_fp16_overflow 0
		.amdhsa_tg_split 0
		.amdhsa_exception_fp_ieee_invalid_op 0
		.amdhsa_exception_fp_denorm_src 0
		.amdhsa_exception_fp_ieee_div_zero 0
		.amdhsa_exception_fp_ieee_overflow 0
		.amdhsa_exception_fp_ieee_underflow 0
		.amdhsa_exception_fp_ieee_inexact 0
		.amdhsa_exception_int_div_zero 0
	.end_amdhsa_kernel

amdhsa.kernels:
  - .agpr_count:     0
    .args:
      - .actual_access:  read_only
        .address_space:  global
        .offset:         0
        .size:           8
        .value_kind:     global_buffer
      - .actual_access:  write_only
        .address_space:  global
        .offset:         8
        .size:           8
        .value_kind:     global_buffer
      - .actual_access:  read_only
        .address_space:  global
        .offset:         16
        .size:           8
        .value_kind:     global_buffer
      - .actual_access:  write_only
        .address_space:  global
        .offset:         24
        .size:           8
        .value_kind:     global_buffer
    .group_segment_fixed_size: 0
    .kernarg_segment_align: 8
    .kernarg_segment_size: 32
    .language:       OpenCL C
    .language_version:
      - 2
      - 0
    .max_flat_workgroup_size: 512
    .name:           _Z9prep_rowsPKfPcS0_S1_
    .private_segment_fixed_size: 0
    .sgpr_count:     28
    .sgpr_spill_count: 0
    .symbol:         _Z9prep_rowsPKfPcS0_S1_.kd
    .uniform_work_group_size: 1
    .uses_dynamic_stack: false
    .vgpr_count:     50
    .vgpr_spill_count: 0
    .wavefront_size: 64
  - .agpr_count:     0
    .args:
      - .address_space:  global
        .offset:         0
        .size:           8
        .value_kind:     global_buffer
      - .address_space:  global
        .offset:         8
        .size:           8
        .value_kind:     global_buffer
      - .actual_access:  write_only
        .address_space:  global
        .offset:         16
        .size:           8
        .value_kind:     global_buffer
    .group_segment_fixed_size: 0
    .kernarg_segment_align: 8
    .kernarg_segment_size: 24
    .language:       OpenCL C
    .language_version:
      - 2
      - 0
    .max_flat_workgroup_size: 512
    .name:           _Z8knn_gemmPKcS0_Pi
    .private_segment_fixed_size: 0
    .sgpr_count:     78
    .sgpr_spill_count: 0
    .symbol:         _Z8knn_gemmPKcS0_Pi.kd
    .uniform_work_group_size: 1
    .uses_dynamic_stack: false
    .vgpr_count:     232
    .vgpr_spill_count: 0
    .wavefront_size: 64
  - .agpr_count:     0
    .args:
      - .actual_access:  read_only
        .address_space:  global
        .offset:         0
        .size:           8
        .value_kind:     global_buffer
      - .actual_access:  read_only
        .address_space:  global
        .offset:         8
        .size:           8
        .value_kind:     global_buffer
      - .actual_access:  read_only
        .address_space:  global
        .offset:         16
        .size:           8
        .value_kind:     global_buffer
      - .actual_access:  read_only
        .address_space:  global
        .offset:         24
        .size:           8
        .value_kind:     global_buffer
      - .actual_access:  write_only
        .address_space:  global
        .offset:         32
        .size:           8
        .value_kind:     global_buffer
    .group_segment_fixed_size: 6752
    .kernarg_segment_align: 8
    .kernarg_segment_size: 40
    .language:       OpenCL C
    .language_version:
      - 2
      - 0
    .max_flat_workgroup_size: 256
    .name:           _Z10knn_selectPKiPKfS2_S2_Pf
    .private_segment_fixed_size: 0
    .sgpr_count:     35
    .sgpr_spill_count: 0
    .symbol:         _Z10knn_selectPKiPKfS2_S2_Pf.kd
    .uniform_work_group_size: 1
    .uses_dynamic_stack: false
    .vgpr_count:     124
    .vgpr_spill_count: 0
    .wavefront_size: 64
